# baseline (speedup 1.0000x reference)
_Z12final_kernelPKfS0_Pfi:
	s_load_dwordx2 s[2:3], s[0:1], 0x8
	s_load_dwordx2 s[14:15], s[0:1], 0x0
	s_load_dwordx2 s[16:17], s[0:1], 0x10
	v_and_b32_e32 v35, 63, v0
	v_lshlrev_b32_e32 v35, 2, v35
	v_lshlrev_b32_e32 v1, 4, v0
	v_lshlrev_b32_e32 v2, 2, v0
	v_cmp_gt_u32_e32 vcc, 0x140, v0
	s_mov_b32 s6, 0xf800000
	v_mov_b32_e32 v3, 0x260
	s_mov_b64 s[18:19], vcc
	s_waitcnt lgkmcnt(0)
	global_load_dword v35, v35, s[14:15]
	s_add_u32 s20, s2, 0x4000
	s_addc_u32 s21, s3, 0
	s_add_u32 s22, s2, 0x8000
	s_addc_u32 s23, s3, 0
	s_add_u32 s24, s2, 0xc000
	s_addc_u32 s25, s3, 0
	s_add_u32 s26, s2, 0x10000
	s_addc_u32 s27, s3, 0
	s_add_u32 s28, s2, 0x14000
	s_addc_u32 s29, s3, 0
	s_add_u32 s30, s2, 0x18000
	s_addc_u32 s31, s3, 0
	global_load_dwordx4 v[36:39], v1, s[2:3]
	global_load_dwordx4 v[40:43], v1, s[20:21]
	global_load_dwordx4 v[44:47], v1, s[22:23]
	global_load_dwordx4 v[48:51], v1, s[24:25]
	global_load_dwordx4 v[52:55], v1, s[26:27]
	global_load_dwordx4 v[56:59], v1, s[28:29]
	s_and_saveexec_b64 s[32:33], s[18:19]
	s_cbranch_execz .Lfk_nol6
	global_load_dwordx4 v[60:63], v1, s[30:31]
.Lfk_nol6:
	s_mov_b64 exec, s[32:33]
	s_waitcnt vmcnt(0)
	v_add_f32_e32 v64, v36, v37
	v_add_f32_e32 v68, v40, v41
	v_add_f32_e32 v72, v44, v45
	v_add_f32_e32 v76, v48, v49
	v_add_f32_e32 v80, v52, v53
	v_add_f32_e32 v84, v56, v57
	v_add_f32_e32 v88, v60, v61
	v_add_f32_e32 v65, v38, v39
	v_add_f32_e32 v69, v42, v43
	v_add_f32_e32 v73, v46, v47
	v_add_f32_e32 v77, v50, v51
	v_add_f32_e32 v81, v54, v55
	v_add_f32_e32 v85, v58, v59
	v_add_f32_e32 v89, v62, v63
	v_add_f32_e32 v64, v64, v65
	v_add_f32_e32 v68, v68, v69
	v_add_f32_e32 v72, v72, v73
	v_add_f32_e32 v76, v76, v77
	v_add_f32_e32 v80, v80, v81
	v_add_f32_e32 v84, v84, v85
	v_add_f32_e32 v88, v88, v89
	v_mul_f32_e32 v65, 0x4f800000, v64
	v_mul_f32_e32 v69, 0x4f800000, v68
	v_mul_f32_e32 v73, 0x4f800000, v72
	v_mul_f32_e32 v77, 0x4f800000, v76
	v_mul_f32_e32 v81, 0x4f800000, v80
	v_mul_f32_e32 v85, 0x4f800000, v84
	v_mul_f32_e32 v89, 0x4f800000, v88
	v_cmp_gt_f32_e64 s[34:35], s6, v64
	v_cmp_gt_f32_e64 s[38:39], s6, v68
	v_cmp_gt_f32_e64 s[42:43], s6, v72
	v_cmp_gt_f32_e64 s[46:47], s6, v76
	v_cmp_gt_f32_e64 s[50:51], s6, v80
	v_cmp_gt_f32_e64 s[54:55], s6, v84
	v_cmp_gt_f32_e64 s[58:59], s6, v88
	v_cndmask_b32_e64 v65, v64, v65, s[34:35]
	v_cndmask_b32_e64 v69, v68, v69, s[38:39]
	v_cndmask_b32_e64 v73, v72, v73, s[42:43]
	v_cndmask_b32_e64 v77, v76, v77, s[46:47]
	v_cndmask_b32_e64 v81, v80, v81, s[50:51]
	v_cndmask_b32_e64 v85, v84, v85, s[54:55]
	v_cndmask_b32_e64 v89, v88, v89, s[58:59]
	v_sqrt_f32_e32 v64, v65
	v_sqrt_f32_e32 v68, v69
	v_sqrt_f32_e32 v72, v73
	v_sqrt_f32_e32 v76, v77
	v_sqrt_f32_e32 v80, v81
	v_sqrt_f32_e32 v84, v85
	v_sqrt_f32_e32 v88, v89
	v_add_u32_e32 v66, -1, v64
	v_add_u32_e32 v70, -1, v68
	v_add_u32_e32 v74, -1, v72
	v_add_u32_e32 v78, -1, v76
	v_add_u32_e32 v82, -1, v80
	v_add_u32_e32 v86, -1, v84
	v_add_u32_e32 v90, -1, v88
	v_fma_f32 v67, -v66, v64, v65
	v_fma_f32 v71, -v70, v68, v69
	v_fma_f32 v75, -v74, v72, v73
	v_fma_f32 v79, -v78, v76, v77
	v_fma_f32 v83, -v82, v80, v81
	v_fma_f32 v87, -v86, v84, v85
	v_fma_f32 v91, -v90, v88, v89
	v_cmp_ge_f32_e64 s[36:37], 0, v67
	v_cmp_ge_f32_e64 s[40:41], 0, v71
	v_cmp_ge_f32_e64 s[44:45], 0, v75
	v_cmp_ge_f32_e64 s[48:49], 0, v79
	v_cmp_ge_f32_e64 s[52:53], 0, v83
	v_cmp_ge_f32_e64 s[56:57], 0, v87
	v_cmp_ge_f32_e64 s[60:61], 0, v91
	v_add_u32_e32 v67, 1, v64
	v_add_u32_e32 v71, 1, v68
	v_add_u32_e32 v75, 1, v72
	v_add_u32_e32 v79, 1, v76
	v_add_u32_e32 v83, 1, v80
	v_add_u32_e32 v87, 1, v84
	v_add_u32_e32 v91, 1, v88
	v_cndmask_b32_e64 v66, v64, v66, s[36:37]
	v_cndmask_b32_e64 v70, v68, v70, s[40:41]
	v_cndmask_b32_e64 v74, v72, v74, s[44:45]
	v_cndmask_b32_e64 v78, v76, v78, s[48:49]
	v_cndmask_b32_e64 v82, v80, v82, s[52:53]
	v_cndmask_b32_e64 v86, v84, v86, s[56:57]
	v_cndmask_b32_e64 v90, v88, v90, s[60:61]
	v_fma_f32 v64, -v67, v64, v65
	v_fma_f32 v68, -v71, v68, v69
	v_fma_f32 v72, -v75, v72, v73
	v_fma_f32 v76, -v79, v76, v77
	v_fma_f32 v80, -v83, v80, v81
	v_fma_f32 v84, -v87, v84, v85
	v_fma_f32 v88, -v91, v88, v89
	v_cmp_lt_f32_e64 s[36:37], 0, v64
	v_cmp_lt_f32_e64 s[40:41], 0, v68
	v_cmp_lt_f32_e64 s[44:45], 0, v72
	v_cmp_lt_f32_e64 s[48:49], 0, v76
	v_cmp_lt_f32_e64 s[52:53], 0, v80
	v_cmp_lt_f32_e64 s[56:57], 0, v84
	v_cmp_lt_f32_e64 s[60:61], 0, v88
	v_cndmask_b32_e64 v64, v66, v67, s[36:37]
	v_cndmask_b32_e64 v68, v70, v71, s[40:41]
	v_cndmask_b32_e64 v72, v74, v75, s[44:45]
	v_cndmask_b32_e64 v76, v78, v79, s[48:49]
	v_cndmask_b32_e64 v80, v82, v83, s[52:53]
	v_cndmask_b32_e64 v84, v86, v87, s[56:57]
	v_cndmask_b32_e64 v88, v90, v91, s[60:61]
	v_mul_f32_e32 v66, 0x37800000, v64
	v_mul_f32_e32 v70, 0x37800000, v68
	v_mul_f32_e32 v74, 0x37800000, v72
	v_mul_f32_e32 v78, 0x37800000, v76
	v_mul_f32_e32 v82, 0x37800000, v80
	v_mul_f32_e32 v86, 0x37800000, v84
	v_mul_f32_e32 v90, 0x37800000, v88
	v_cndmask_b32_e64 v66, v64, v66, s[34:35]
	v_cndmask_b32_e64 v70, v68, v70, s[38:39]
	v_cndmask_b32_e64 v74, v72, v74, s[42:43]
	v_cndmask_b32_e64 v78, v76, v78, s[46:47]
	v_cndmask_b32_e64 v82, v80, v82, s[50:51]
	v_cndmask_b32_e64 v86, v84, v86, s[54:55]
	v_cndmask_b32_e64 v90, v88, v90, s[58:59]
	v_cmp_class_f32_e64 s[34:35], v65, v3
	v_cmp_class_f32_e64 s[38:39], v69, v3
	v_cmp_class_f32_e64 s[42:43], v73, v3
	v_cmp_class_f32_e64 s[46:47], v77, v3
	v_cmp_class_f32_e64 s[50:51], v81, v3
	v_cmp_class_f32_e64 s[54:55], v85, v3
	v_cmp_class_f32_e64 s[58:59], v89, v3
	v_cndmask_b32_e64 v65, v66, v65, s[34:35]
	v_cndmask_b32_e64 v69, v70, v69, s[38:39]
	v_cndmask_b32_e64 v73, v74, v73, s[42:43]
	v_cndmask_b32_e64 v77, v78, v77, s[46:47]
	v_cndmask_b32_e64 v81, v82, v81, s[50:51]
	v_cndmask_b32_e64 v85, v86, v85, s[54:55]
	v_cndmask_b32_e64 v89, v90, v89, s[58:59]
	ds_write_b32 v2, v65
	ds_write_b32 v2, v69 offset:4096
	ds_write_b32 v2, v73 offset:8192
	ds_write_b32 v2, v77 offset:12288
	ds_write_b32 v2, v81 offset:16384
	ds_write_b32 v2, v85 offset:20480
	s_and_saveexec_b64 s[32:33], s[18:19]
	ds_write_b32 v2, v89 offset:24576
	s_mov_b64 exec, s[32:33]
	s_mov_b64 s[4:5], exec

	.amdhsa_kernel _Z12final_kernelPKfS0_Pfi
		.amdhsa_group_segment_fixed_size 26116
		.amdhsa_private_segment_fixed_size 0
		.amdhsa_kernarg_size 28
		.amdhsa_user_sgpr_count 2
		.amdhsa_user_sgpr_dispatch_ptr 0
		.amdhsa_user_sgpr_queue_ptr 0
		.amdhsa_user_sgpr_kernarg_segment_ptr 1
		.amdhsa_user_sgpr_dispatch_id 0
		.amdhsa_user_sgpr_kernarg_preload_length 0
		.amdhsa_user_sgpr_kernarg_preload_offset 0
		.amdhsa_user_sgpr_private_segment_size 0
		.amdhsa_uses_dynamic_stack 0
		.amdhsa_enable_private_segment 0
		.amdhsa_system_sgpr_workgroup_id_x 1
		.amdhsa_system_sgpr_workgroup_id_y 0
		.amdhsa_system_sgpr_workgroup_id_z 0
		.amdhsa_system_sgpr_workgroup_info 0
		.amdhsa_system_vgpr_workitem_id 0
		.amdhsa_next_free_vgpr 92
		.amdhsa_next_free_sgpr 64
		.amdhsa_accum_offset 92
		.amdhsa_reserve_vcc 1
		.amdhsa_float_round_mode_32 0
		.amdhsa_float_round_mode_16_64 0
		.amdhsa_float_denorm_mode_32 3
		.amdhsa_float_denorm_mode_16_64 3
		.amdhsa_dx10_clamp 1
		.amdhsa_ieee_mode 1
		.amdhsa_fp16_overflow 0
		.amdhsa_tg_split 0
		.amdhsa_exception_fp_ieee_invalid_op 0
		.amdhsa_exception_fp_denorm_src 0
		.amdhsa_exception_fp_ieee_div_zero 0
		.amdhsa_exception_fp_ieee_overflow 0
		.amdhsa_exception_fp_ieee_underflow 0
		.amdhsa_exception_fp_ieee_inexact 0
		.amdhsa_exception_int_div_zero 0
	.end_amdhsa_kernel

amdhsa.kernels:
  - .agpr_count:     240
    .args:
      - .actual_access:  read_only
        .address_space:  global
        .offset:         0
        .size:           8
        .value_kind:     global_buffer
      - .actual_access:  read_only
        .address_space:  global
        .offset:         8
        .size:           8
        .value_kind:     global_buffer
      - .actual_access:  read_only
        .address_space:  global
        .offset:         16
        .size:           8
        .value_kind:     global_buffer
      - .address_space:  global
        .offset:         24
        .size:           8
        .value_kind:     global_buffer
      - .actual_access:  write_only
        .address_space:  global
        .offset:         32
        .size:           8
        .value_kind:     global_buffer
    .group_segment_fixed_size: 158272
    .kernarg_segment_align: 8
    .kernarg_segment_size: 40
    .language:       OpenCL C
    .language_version:
      - 2
      - 0
    .max_flat_workgroup_size: 256
    .name:           _Z11jacobi_mainPKfS0_S0_PyPf
    .private_segment_fixed_size: 0
    .sgpr_count:     80
    .sgpr_spill_count: 0
    .symbol:         _Z11jacobi_mainPKfS0_S0_PyPf.kd
    .uniform_work_group_size: 1
    .uses_dynamic_stack: false
    .vgpr_count:     496
    .vgpr_spill_count: 0
    .wavefront_size: 64
  - .agpr_count:     0
    .args:
      - .actual_access:  read_only
        .address_space:  global
        .offset:         0
        .size:           8
        .value_kind:     global_buffer
      - .actual_access:  read_only
        .address_space:  global
        .offset:         8
        .size:           8
        .value_kind:     global_buffer
      - .actual_access:  write_only
        .address_space:  global
        .offset:         16
        .size:           8
        .value_kind:     global_buffer
      - .offset:         24
        .size:           4
        .value_kind:     by_value
    .group_segment_fixed_size: 26116
    .kernarg_segment_align: 8
    .kernarg_segment_size: 28
    .language:       OpenCL C
    .language_version:
      - 2
      - 0
    .max_flat_workgroup_size: 1024
    .name:           _Z12final_kernelPKfS0_Pfi
    .private_segment_fixed_size: 0
    .sgpr_count:     70
    .sgpr_spill_count: 0
    .symbol:         _Z12final_kernelPKfS0_Pfi.kd
    .uniform_work_group_size: 1
    .uses_dynamic_stack: false
    .vgpr_count:     92
    .vgpr_spill_count: 0
    .wavefront_size: 64
